# v27: v25 + spatial gating: next unit's z(v) and u rows prefetched by LDS-DMA into per-wave LDS slots during the current unit, picked up by ds_read
# baseline (speedup 1.0000x reference)
; #define LAS __attribute__((address_space(3)))
; __device__ __forceinline__ void sg_phase(const Frame& F, const KArgs& a, const int u_first, const int u_count) {
;     unsigned char* ws = F.ws; const int tid = F.tid, lane = F.lane, w = F.wave, tl = lane & 15, kq = lane >> 4;
;     LAS f32x2* st = (LAS f32x2*)F.lds;
;     LAS unsigned short* vt = (LAS unsigned short*)(F.lds + 1024);
;     const bf16* ZU = (const bf16*)(ws + WS_ZU); const bf16* ZV = (const bf16*)(ws + WS_ZV); const float* ZST = (const float*)(ws + WS_ZST); bf16* AS = (bf16*)(ws + WS_AS);
;     const float* ln_g = a.in[5]; const float* ln_b = a.in[6]; const float* w_sp = a.in[7]; const float* b_sp = a.in[8];
;     for (int uu = 0; uu < u_count; ++uu) { const int u = u_first + uu;
;         const int chunk = u >> 3, g = u & 7, t0 = chunk * SGC;
;         const int t = 16 * w + tl;
;         f32x4 zst[8];
;         if (tid < 128) { const f32x4* p = (const f32x4*)(ZST + (size_t)(t0 + tid) * 32);
; #pragma unroll
;             for (int i = 0; i < 8; ++i) zst[i] = p[i]; }
;         const int s_ = tid >> 2, c0 = (tid & 3) * 32; const bf16* src = ZV + (size_t)(t0 + s_) * SGW + g * 128 + c0;
;         u32x4 zraw[4]; f32x4 lg[4][2], lb[4][2];
; #pragma unroll
;         for (int q = 0; q < 4; ++q) { zraw[q] = ((const u32x4*)src)[q];
;             lg[q][0] = *(const f32x4*)(ln_g + g * 128 + c0 + 8 * q); lg[q][1] = *(const f32x4*)(ln_g + g * 128 + c0 + 8 * q + 4); lb[q][0] = *(const f32x4*)(ln_b + g * 128 + c0 + 8 * q); lb[q][1] = *(const f32x4*)(ln_b + g * 128 + c0 + 8 * q + 4); }
;         f32x4 wraw[4][2];
; #pragma unroll
;         for (int ks = 0; ks < 4; ++ks) { const float* wp = w_sp + ((size_t)(g * 128 + t) * 128 + 32 * ks + 8 * kq); if (ks <= (w >> 1)) { wraw[ks][0] = *(const f32x4*)wp; wraw[ks][1] = *(const f32x4*)(wp + 4); } else { wraw[ks][0] = (f32x4){0.f, 0.f, 0.f, 0.f}; wraw[ks][1] = (f32x4){0.f, 0.f, 0.f, 0.f}; } }
;         u32x2 uraw[8];
; #pragma unroll
;         for (int j = 0; j < 8; ++j) uraw[j] = *(const u32x2*)(ZU + (size_t)(t0 + t) * SGW + g * 128 + 16 * j + 4 * kq);
.LBB0_802:
	s_waitcnt vmcnt(0)
	v_lshrrev_b32_e32 v4, 4, v198
	s_waitcnt lgkmcnt(0)
	v_and_b32_e32 v3, 15, v0
	v_readlane_b32 s4, v252, 6
	v_lshlrev_b32_e32 v6, 3, v4
	v_lshl_or_b32 v176, s75, 4, v3
	v_readlane_b32 s8, v252, 10
	v_readlane_b32 s9, v252, 11
	v_or_b32_e32 v8, 2, v6
	v_readlane_b32 s10, v252, 12
	v_readlane_b32 s11, v252, 13
	v_cmp_gt_u32_e64 s[8:9], v8, v176
	v_or_b32_e32 v8, 3, v6
	v_and_b32_e32 v5, 3, v0
	v_readlane_b32 s12, v252, 14
	v_readlane_b32 s13, v252, 15
	v_cmp_gt_u32_e64 s[10:11], v8, v176
	v_or_b32_e32 v8, 4, v6
	v_mov_b32_e32 v147, 0
	v_lshlrev_b32_e32 v146, 7, v5
	v_readlane_b32 s14, v252, 16
	v_readlane_b32 s15, v252, 17
	v_cmp_gt_u32_e64 s[12:13], v8, v176
	v_or_b32_e32 v8, 5, v6
	v_readlane_b32 s16, v252, 18
	v_readlane_b32 s17, v252, 19
	v_lshl_add_u64 v[148:149], s[14:15], 0, v[146:147]
	v_cmp_gt_u32_e64 s[14:15], v8, v176
	v_or_b32_e32 v8, 6, v6
	v_readlane_b32 s18, v252, 20
	v_readlane_b32 s19, v252, 21
	v_lshl_add_u64 v[150:151], s[16:17], 0, v[146:147]
	v_lshlrev_b32_e32 v146, 5, v4
	v_cmp_gt_u32_e64 s[16:17], v8, v176
	v_or_b32_e32 v8, 7, v6
	s_movk_i32 s20, 0x110
	v_lshl_add_u64 v[152:153], s[18:19], 0, v[146:147]
	v_cmp_gt_u32_e64 s[18:19], v8, v176
	v_mad_u32_u24 v3, v3, s20, 0
	v_and_b32_e32 v8, 48, v198
	v_writelane_b32 v251, s71, 13
	v_add_u32_e32 v180, v3, v8
	v_xad_u32 v181, v8, 32, v3
	v_or_b32_e32 v8, 32, v6
	v_writelane_b32 v251, s75, 14
	v_cmp_gt_u32_e64 s[20:21], v8, v176
	v_or_b32_e32 v8, 33, v6
	s_add_u32 s0, s72, 0xb600000
	v_writelane_b32 v251, s20, 7
	s_addc_u32 s1, s73, 0
	s_add_u32 s80, s72, 0xd600000
	v_writelane_b32 v251, s21, 8
	v_cmp_gt_u32_e64 s[20:21], v8, v176
	v_or_b32_e32 v8, 34, v6
	s_addc_u32 s81, s73, 0
	v_writelane_b32 v251, s20, 16
	s_add_u32 s84, s72, 0xf600000
	s_addc_u32 s85, s73, 0
	v_writelane_b32 v251, s21, 17
	v_cmp_gt_u32_e64 s[20:21], v8, v176
	v_or_b32_e32 v8, 35, v6
	v_readlane_b32 s4, v252, 63
	v_writelane_b32 v251, s20, 22
	v_lshrrev_b32_e32 v177, 2, v0
	s_cmpk_gt_u32 s4, 0x7f
	v_writelane_b32 v251, s21, 23
	v_cmp_gt_u32_e64 s[20:21], v8, v176
	v_or_b32_e32 v8, 36, v6
	v_lshlrev_b32_e32 v2, 5, v5
	v_writelane_b32 v251, s20, 24
	v_readlane_b32 s5, v252, 7
	v_readlane_b32 s6, v252, 8
	v_writelane_b32 v251, s21, 25
	v_cmp_gt_u32_e64 s[20:21], v8, v176
	v_or_b32_e32 v8, 37, v6
	v_readlane_b32 s7, v252, 9
	v_writelane_b32 v251, s20, 26
	v_lshlrev_b32_e32 v7, 1, v177
	s_cselect_b64 s[82:83], -1, 0
	v_writelane_b32 v251, s21, 27
	v_cmp_gt_u32_e64 s[20:21], v8, v176
	v_or_b32_e32 v8, 38, v6
	v_cmp_gt_u32_e64 s[34:35], v8, v176
	v_or_b32_e32 v8, 39, v6
	v_cmp_gt_u32_e64 s[94:95], v8, v176
	v_or_b32_e32 v8, 64, v6
	v_writelane_b32 v251, s20, 28
	v_cmp_gt_u32_e64 s[96:97], v8, v176
	v_or_b32_e32 v8, 0x41, v6
	v_writelane_b32 v251, s21, 29
	v_cmp_gt_u32_e64 s[20:21], v8, v176
	v_or_b32_e32 v8, 0x42, v6
	v_cmp_gt_u32_e64 s[22:23], v8, v176
	v_or_b32_e32 v8, 0x43, v6
	v_cmp_gt_u32_e64 s[24:25], v8, v176
	v_or_b32_e32 v8, 0x44, v6
	v_cmp_gt_u32_e64 s[26:27], v8, v176
	v_or_b32_e32 v8, 0x45, v6
	v_cmp_gt_u32_e64 s[28:29], v8, v176
	v_or_b32_e32 v8, 0x46, v6
	v_cmp_gt_u32_e64 s[30:31], v8, v176
	v_or_b32_e32 v8, 0x47, v6
	v_cmp_gt_u32_e64 s[52:53], v8, v176
	v_or_b32_e32 v8, 0x60, v6
	v_cmp_gt_u32_e64 s[54:55], v8, v176
	v_or_b32_e32 v8, 0x61, v6
	v_cmp_gt_u32_e64 s[56:57], v8, v176
	v_or_b32_e32 v8, 0x62, v6
	v_cmp_gt_u32_e64 s[58:59], v8, v176
	v_or_b32_e32 v8, 0x63, v6
	v_cmp_gt_u32_e64 s[60:61], v8, v176
	v_or_b32_e32 v8, 0x64, v6
	v_cmp_gt_u32_e64 s[62:63], v8, v176
	v_or_b32_e32 v8, 0x65, v6
	v_cmp_gt_u32_e64 s[64:65], v8, v176
	v_or_b32_e32 v8, 0x66, v6
	v_cmp_gt_u32_e64 s[66:67], v8, v176
	v_or_b32_e32 v8, 0x67, v6
	s_cmpk_gt_u32 s4, 0xff
	v_cmp_gt_u32_e64 s[68:69], v8, v176
	s_movk_i32 s33, 0x58
	v_mov_b32_e32 v8, 0x60
	s_movk_i32 s2, 0x80
	v_lshlrev_b32_e32 v4, 2, v4
	v_xad_u32 v7, v2, v7, 0
	s_cselect_b64 s[86:87], -1, 0
	s_cmpk_gt_u32 s4, 0x17f
	v_mul_u32_u24_e32 v5, 0x2200, v5
	v_cmp_gt_u32_e64 s[4:5], v6, v176
	v_cmp_lt_u32_e64 s[6:7], v6, v176
	v_bitop3_b32 v6, v6, s33, v8 bitop3:0xc8
	v_cmp_gt_u32_e64 s[2:3], s2, v0
	s_mov_b32 s79, 0
	v_lshl_add_u32 v178, v0, 3, 0
	v_lshl_add_u32 v179, v177, 3, 0
	s_cselect_b64 s[88:89], -1, 0
	v_lshl_add_u32 v182, v6, 1, v3
	s_lshl_b32 s33, s70, 7
	s_lshl_b32 s90, s70, 4
	v_lshlrev_b32_e32 v154, 1, v2
	v_lshlrev_b32_e32 v156, 1, v4
	s_movk_i32 s91, 0x7fff
	v_add_u32_e32 v183, v7, v5
	v_lshlrev_b32_e32 v242, 3, v198
	v_and_b32_e32 v240, 3, v0
	v_add_u32_e32 v241, 0xa000, v242
	v_lshlrev_b32_e32 v240, 7, v240
	v_add_u32_e32 v240, 0xa000, v240
	v_lshlrev_b32_e32 v243, 4, v198
	v_readfirstlane_b32 s98, v0
	s_nop 3
	s_lshr_b32 s98, s98, 6
	s_lshl_b32 s98, s98, 13
	s_add_i32 s98, s98, 0xa800
	v_add_u32_e32 v243, s98, v243
	s_and_b32 s98, s90, 0xffffff80
	s_and_b32 s99, s33, 0x380
	s_lshl_b32 s100, s99, 1
	s_mov_b32 s101, 0
	v_add_u32_e32 v200, s98, v177
	v_ashrrev_i32_e32 v201, 31, v200
	v_lshlrev_b64 v[200:201], 11, v[200:201]
	v_lshl_add_u64 v[200:201], s[80:81], 0, v[200:201]
	v_lshl_add_u64 v[200:201], v[200:201], 0, s[100:101]
	v_mov_b32_e32 v202, v154
	v_mov_b32_e32 v203, 0
	v_lshl_add_u64 v[200:201], v[200:201], 0, v[202:203]
	v_add_u32_e32 v204, s98, v176
	v_ashrrev_i32_e32 v205, 31, v204
	v_lshlrev_b64 v[204:205], 11, v[204:205]
	v_lshl_add_u64 v[204:205], s[0:1], 0, v[204:205]
	v_lshl_add_u64 v[204:205], v[204:205], 0, s[100:101]
	v_mov_b32_e32 v202, v156
	v_lshl_add_u64 v[204:205], v[204:205], 0, v[202:203]
	v_lshl_add_u64 v[204:205], v[204:205], 0, v[202:203]
	v_readfirstlane_b32 s98, v0
	s_nop 3
	s_lshr_b32 s98, s98, 6
	s_lshl_b32 s98, s98, 13
	s_add_i32 s98, s98, 0xa800
	v_mov_b32_e32 v206, 16
	v_mov_b32_e32 v207, 0
	v_mov_b32_e32 v208, 64
	v_mov_b32_e32 v209, 0
	s_add_i32 m0, s98, 0xc00
	s_nop 0
	global_load_lds_dwordx4 v[200:201], off
	v_lshl_add_u64 v[200:201], v[200:201], 0, v[206:207]
	s_add_i32 m0, s98, 0x800
	s_nop 0
	global_load_lds_dwordx4 v[200:201], off
	v_lshl_add_u64 v[200:201], v[200:201], 0, v[206:207]
	s_add_i32 m0, s98, 0x400
	s_nop 0
	global_load_lds_dwordx4 v[200:201], off
	v_lshl_add_u64 v[200:201], v[200:201], 0, v[206:207]
	s_add_i32 m0, s98, 0x0
	s_nop 0
	global_load_lds_dwordx4 v[200:201], off
	s_add_i32 m0, s98, 0x1000
	s_nop 0
	global_load_lds_dwordx4 v[204:205], off
	v_lshl_add_u64 v[204:205], v[204:205], 0, v[208:209]
	s_add_i32 m0, s98, 0x1400
	s_nop 0
	global_load_lds_dwordx4 v[204:205], off
	v_lshl_add_u64 v[204:205], v[204:205], 0, v[208:209]
	s_add_i32 m0, s98, 0x1800
	s_nop 0
	global_load_lds_dwordx4 v[204:205], off
	v_lshl_add_u64 v[204:205], v[204:205], 0, v[208:209]
	s_add_i32 m0, s98, 0x1c00
	s_nop 0
	global_load_lds_dwordx4 v[204:205], off
	s_waitcnt vmcnt(0)
	s_branch .LBB0_804
; __device__ __forceinline__ unsigned cvt_pk_bf16(float lo, float hi) { unsigned r; asm volatile("v_cvt_pk_bf16_f32 %0, %1, %2" : "=v"(r) : "v"(lo), "v"(hi)); return r; }
; __device__ __forceinline__ void sg_phase(const Frame& F, const KArgs& a, const int u_first, const int u_count) {
;     ...
;     for (int uu = 0; uu < u_count; ++uu) { const int u = u_first + uu;
;         const int chunk = u >> 3, g = u & 7, t0 = chunk * SGC;
;         const int t = 16 * w + tl;
;         f32x4 zst[8];
;         if (tid < 128) { const f32x4* p = (const f32x4*)(ZST + (size_t)(t0 + tid) * 32);
; #pragma unroll
;             for (int i = 0; i < 8; ++i) zst[i] = p[i]; }
;         const int s_ = tid >> 2, c0 = (tid & 3) * 32; const bf16* src = ZV + (size_t)(t0 + s_) * SGW + g * 128 + c0;
;         u32x4 zraw[4]; f32x4 lg[4][2], lb[4][2];
; #pragma unroll
;         for (int q = 0; q < 4; ++q) { zraw[q] = ((const u32x4*)src)[q];
;             lg[q][0] = *(const f32x4*)(ln_g + g * 128 + c0 + 8 * q); lg[q][1] = *(const f32x4*)(ln_g + g * 128 + c0 + 8 * q + 4); lb[q][0] = *(const f32x4*)(ln_b + g * 128 + c0 + 8 * q); lb[q][1] = *(const f32x4*)(ln_b + g * 128 + c0 + 8 * q + 4); }
;         f32x4 wraw[4][2];
; #pragma unroll
;         for (int ks = 0; ks < 4; ++ks) { const float* wp = w_sp + ((size_t)(g * 128 + t) * 128 + 32 * ks + 8 * kq); if (ks <= (w >> 1)) { wraw[ks][0] = *(const f32x4*)wp; wraw[ks][1] = *(const f32x4*)(wp + 4); } else { wraw[ks][0] = (f32x4){0.f, 0.f, 0.f, 0.f}; wraw[ks][1] = (f32x4){0.f, 0.f, 0.f, 0.f}; } }
;     ...
; #pragma unroll
;         for (int j = 0; j < 8; ++j) { const int ch = 16 * j + 4 * kq; const u32x2 uu = uraw[j];
;             const float o0 = __builtin_bit_cast(float, uu.x << 16) * (acc[j][0] + bs), o1 = __builtin_bit_cast(float, uu.x & 0xffff0000u) * (acc[j][1] + bs);
;             const float o2 = __builtin_bit_cast(float, uu.y << 16) * (acc[j][2] + bs), o3 = __builtin_bit_cast(float, uu.y & 0xffff0000u) * (acc[j][3] + bs);
;             u32x2 o; o.x = cvt_pk_bf16(o0, o1); o.y = cvt_pk_bf16(o2, o3); *(u32x2*)(AS + (size_t)(t0 + t) * DM + FW + g * 128 + ch) = o; }
;         __syncthreads();
;     }
.LBB0_803:
	s_waitcnt vmcnt(8)
	v_lshlrev_b64 v[34:35], 12, v[174:175]
	v_lshl_add_u64 v[34:35], s[72:73], 0, v[34:35]
	v_lshl_add_u64 v[34:35], v[34:35], 0, s[78:79]
	v_mov_b32_e32 v157, v147
	v_lshl_add_u64 v[34:35], v[34:35], 0, v[156:157]
	s_mov_b64 s[70:71], 0x17800800
	v_lshl_add_u64 v[38:39], v[34:35], 0, s[70:71]
	v_lshl_add_u64 v[38:39], v[38:39], 0, v[156:157]
	v_lshlrev_b32_e32 v34, 16, v170
	v_add_f32_e32 v35, v146, v82
	v_mul_f32_e32 v34, v35, v34
	v_and_b32_e32 v35, 0xffff0000, v170
	v_add_f32_e32 v36, v146, v83
	v_mul_f32_e32 v35, v36, v35
	v_lshlrev_b32_e32 v36, 16, v171
	v_add_f32_e32 v37, v146, v84
	v_mul_f32_e32 v36, v37, v36
	v_and_b32_e32 v37, 0xffff0000, v171
	v_add_f32_e32 v40, v146, v85
	v_mul_f32_e32 v37, v40, v37
	v_cvt_pk_bf16_f32 v170, v34, v35
	v_cvt_pk_bf16_f32 v171, v36, v37
	v_lshlrev_b32_e32 v34, 16, v172
	v_add_f32_e32 v35, v146, v86
	v_mul_f32_e32 v34, v35, v34
	v_and_b32_e32 v35, 0xffff0000, v172
	v_add_f32_e32 v36, v146, v87
	v_mul_f32_e32 v35, v36, v35
	v_lshlrev_b32_e32 v36, 16, v173
	v_add_f32_e32 v37, v146, v88
	v_mul_f32_e32 v36, v37, v36
	v_and_b32_e32 v37, 0xffff0000, v173
	v_add_f32_e32 v40, v146, v89
	v_mul_f32_e32 v37, v40, v37
	v_cvt_pk_bf16_f32 v172, v34, v35
	v_cvt_pk_bf16_f32 v173, v36, v37
	s_nop 0
	s_waitcnt vmcnt(0)
	global_store_dwordx4 v[38:39], v[170:173], off
	v_lshlrev_b32_e32 v34, 16, v166
	v_add_f32_e32 v35, v146, v74
	v_mul_f32_e32 v34, v35, v34
	v_and_b32_e32 v35, 0xffff0000, v166
	v_add_f32_e32 v36, v146, v75
	v_mul_f32_e32 v35, v36, v35
	v_lshlrev_b32_e32 v36, 16, v167
	v_add_f32_e32 v37, v146, v76
	v_mul_f32_e32 v36, v37, v36
	v_and_b32_e32 v37, 0xffff0000, v167
	v_add_f32_e32 v40, v146, v77
	v_mul_f32_e32 v37, v40, v37
	v_cvt_pk_bf16_f32 v166, v34, v35
	v_cvt_pk_bf16_f32 v167, v36, v37
	v_lshlrev_b32_e32 v34, 16, v168
	v_add_f32_e32 v35, v146, v78
	v_mul_f32_e32 v34, v35, v34
	v_and_b32_e32 v35, 0xffff0000, v168
	v_add_f32_e32 v36, v146, v79
	v_mul_f32_e32 v35, v36, v35
	v_lshlrev_b32_e32 v36, 16, v169
	v_add_f32_e32 v37, v146, v80
	v_mul_f32_e32 v36, v37, v36
	v_and_b32_e32 v37, 0xffff0000, v169
	v_add_f32_e32 v40, v146, v81
	v_mul_f32_e32 v37, v40, v37
	v_cvt_pk_bf16_f32 v168, v34, v35
	v_cvt_pk_bf16_f32 v169, v36, v37
	s_nop 0
	global_store_dwordx4 v[38:39], v[166:169], off offset:64
	v_lshlrev_b32_e32 v34, 16, v162
	v_add_f32_e32 v35, v146, v66
	v_mul_f32_e32 v34, v35, v34
	v_and_b32_e32 v35, 0xffff0000, v162
	v_add_f32_e32 v36, v146, v67
	v_mul_f32_e32 v35, v36, v35
	v_lshlrev_b32_e32 v36, 16, v163
	v_add_f32_e32 v37, v146, v68
	v_mul_f32_e32 v36, v37, v36
	v_and_b32_e32 v37, 0xffff0000, v163
	v_add_f32_e32 v40, v146, v69
	v_mul_f32_e32 v37, v40, v37
	v_cvt_pk_bf16_f32 v162, v34, v35
	v_cvt_pk_bf16_f32 v163, v36, v37
	v_lshlrev_b32_e32 v34, 16, v164
	v_add_f32_e32 v35, v146, v70
	v_mul_f32_e32 v34, v35, v34
	v_and_b32_e32 v35, 0xffff0000, v164
	v_add_f32_e32 v36, v146, v71
	v_mul_f32_e32 v35, v36, v35
	v_lshlrev_b32_e32 v36, 16, v165
	v_add_f32_e32 v37, v146, v72
	v_mul_f32_e32 v36, v37, v36
	v_and_b32_e32 v37, 0xffff0000, v165
	v_add_f32_e32 v40, v146, v73
	v_mul_f32_e32 v37, v40, v37
	v_cvt_pk_bf16_f32 v164, v34, v35
	v_cvt_pk_bf16_f32 v165, v36, v37
	s_nop 0
	global_store_dwordx4 v[38:39], v[162:165], off offset:128
	v_lshlrev_b32_e32 v34, 16, v158
	v_add_f32_e32 v35, v146, v58
	v_mul_f32_e32 v34, v35, v34
	v_and_b32_e32 v35, 0xffff0000, v158
	v_add_f32_e32 v36, v146, v59
	v_mul_f32_e32 v35, v36, v35
	v_lshlrev_b32_e32 v36, 16, v159
	v_add_f32_e32 v37, v146, v60
	v_mul_f32_e32 v36, v37, v36
	v_and_b32_e32 v37, 0xffff0000, v159
	v_add_f32_e32 v40, v146, v61
	v_mul_f32_e32 v37, v40, v37
	v_cvt_pk_bf16_f32 v158, v34, v35
	v_cvt_pk_bf16_f32 v159, v36, v37
	v_lshlrev_b32_e32 v34, 16, v160
	v_add_f32_e32 v35, v146, v62
	v_mul_f32_e32 v34, v35, v34
	v_and_b32_e32 v35, 0xffff0000, v160
	v_add_f32_e32 v36, v146, v63
	v_mul_f32_e32 v35, v36, v35
	v_lshlrev_b32_e32 v36, 16, v161
	v_add_f32_e32 v37, v146, v64
	v_mul_f32_e32 v36, v37, v36
	v_and_b32_e32 v37, 0xffff0000, v161
	v_add_f32_e32 v40, v146, v65
	v_mul_f32_e32 v37, v40, v37
	v_cvt_pk_bf16_f32 v160, v34, v35
	v_cvt_pk_bf16_f32 v161, v36, v37
	s_nop 0
	global_store_dwordx4 v[38:39], v[158:161], off offset:192
	v_add_u32_e32 v1, -1, v1
	v_cmp_ne_u32_e32 vcc, 0, v1
	s_addk_i32 s33, 0x80
	s_and_b64 vcc, exec, vcc
	s_add_i32 s90, s90, 16
	s_barrier
	s_cbranch_vccz .LBB0_820
.LBB0_804:
	s_waitcnt vmcnt(4)
	ds_read_b128 v[58:61], v243
	ds_read_b128 v[86:89], v243 offset:1024
	ds_read_b128 v[110:113], v243 offset:2048
	ds_read_b128 v[130:133], v243 offset:3072
	s_and_b32 s76, s90, 0xffffff80
	s_and_saveexec_b64 s[70:71], s[2:3]
	s_cbranch_execz .LBB0_806
	v_or_b32_e32 v2, s76, v0
	v_ashrrev_i32_e32 v3, 31, v2
	v_lshlrev_b64 v[2:3], 7, v[2:3]
	v_lshl_add_u64 v[18:19], s[84:85], 0, v[2:3]
	global_load_dwordx4 v[14:17], v[18:19], off offset:48
	global_load_dwordx4 v[10:13], v[18:19], off offset:32
	global_load_dwordx4 v[6:9], v[18:19], off offset:16
	global_load_dwordx4 v[2:5], v[18:19], off
	global_load_dwordx4 v[30:33], v[18:19], off offset:112
	global_load_dwordx4 v[26:29], v[18:19], off offset:96
	global_load_dwordx4 v[22:25], v[18:19], off offset:80
	s_nop 0
	global_load_dwordx4 v[18:21], v[18:19], off offset:64
.LBB0_806:
	s_or_b64 exec, exec, s[70:71]
	v_add_u32_e32 v34, s76, v177
	v_ashrrev_i32_e32 v35, 31, v34
	v_lshlrev_b64 v[34:35], 11, v[34:35]
	s_and_b32 s72, s33, 0x380
	v_lshl_add_u64 v[34:35], s[80:81], 0, v[34:35]
	s_lshl_b32 s78, s72, 1
	v_lshl_add_u64 v[34:35], v[34:35], 0, s[78:79]
	v_mov_b32_e32 v155, v147
	v_lshl_add_u64 v[34:35], v[34:35], 0, v[154:155]
	s_lshl_b32 s70, s72, 2
	s_mov_b32 s71, s79
	v_lshl_add_u64 v[36:37], v[148:149], 0, s[70:71]
	v_lshl_add_u64 v[38:39], v[150:151], 0, s[70:71]
	v_readlane_b32 s98, v252, 16
	v_readlane_b32 s99, v252, 17
	v_readlane_b32 s100, v252, 18
	v_readlane_b32 s101, v252, 19
	s_add_u32 s98, s98, s70
	s_addc_u32 s99, s99, 0
	s_add_u32 s100, s100, s70
	s_addc_u32 s101, s101, 0
	global_load_dwordx2 v[244:245], v242, s[98:99]
	global_load_dwordx2 v[246:247], v242, s[100:101]
	v_add_u32_e32 v146, s72, v176
	v_lshlrev_b64 v[34:35], 9, v[146:147]
	v_lshl_add_u64 v[158:159], v[152:153], 0, v[34:35]
	global_load_dwordx4 v[62:65], v[158:159], off offset:16
	global_load_dwordx4 v[74:77], v[158:159], off
	v_cndmask_b32_e64 v34, 0, 1, s[82:83]
	v_mov_b32_e32 v42, 0
	v_cmp_ne_u32_e64 s[74:75], 1, v34
	s_andn2_b64 vcc, exec, s[82:83]
	v_mov_b32_e32 v50, 0
	v_mov_b32_e32 v51, 0
	v_mov_b32_e32 v52, 0
	v_mov_b32_e32 v53, 0
	v_mov_b32_e32 v54, 0
	v_mov_b32_e32 v55, 0
	v_mov_b32_e32 v56, 0
	v_mov_b32_e32 v57, 0
	s_cbranch_vccnz .LBB0_808
	global_load_dwordx4 v[50:53], v[158:159], off offset:144
	global_load_dwordx4 v[54:57], v[158:159], off offset:128

; __device__ __forceinline__ void sg_phase(const Frame& F, const KArgs& a, const int u_first, const int u_count) {
;     ...
;         u32x2 uraw[8];
; #pragma unroll
;         for (int j = 0; j < 8; ++j) uraw[j] = *(const u32x2*)(ZU + (size_t)(t0 + t) * SGW + g * 128 + 16 * j + 4 * kq);
;         const float bs = b_sp[g * 128 + t];
;         if (tid < 128) { float S = 0.f, Q = 0.f;
; #pragma unroll
;             for (int i = 0; i < 8; ++i) { const f32x4 v = zst[i]; S += v[0] + v[2]; Q += v[1] + v[3]; }
;             const float mu = S * (1.f / SGW), var = fmaxf(Q * (1.f / SGW) - mu * mu, 0.f); st[tid] = (f32x2){mu, rsqrtf(var + LN_EPS)}; }
;         __syncthreads();
.LBB0_812:
	v_add_u32_e32 v174, s76, v176
	v_ashrrev_i32_e32 v175, 31, v174
	v_lshlrev_b64 v[158:159], 11, v[174:175]
	v_lshl_add_u64 v[158:159], s[0:1], 0, v[158:159]
	v_lshl_add_u64 v[158:159], v[158:159], 0, s[78:79]
	v_mov_b32_e32 v157, v147
	v_lshl_add_u64 v[158:159], v[158:159], 0, v[156:157]
	v_lshl_add_u64 v[158:159], v[158:159], 0, v[156:157]
	ds_read_b128 v[170:173], v243 offset:4096
	ds_read_b128 v[166:169], v243 offset:5120
	ds_read_b128 v[162:165], v243 offset:6144
	ds_read_b128 v[158:161], v243 offset:7168
	v_readlane_b32 s36, v252, 47
	v_readlane_b32 s37, v252, 48
	v_readlane_b32 s38, v252, 49
	v_readlane_b32 s39, v252, 50
	v_lshl_add_u64 v[184:185], v[146:147], 2, s[36:37]
	global_load_dword v146, v[184:185], off
	v_readlane_b32 s40, v252, 51
	v_readlane_b32 s41, v252, 52
	v_readlane_b32 s42, v252, 53
	v_readlane_b32 s43, v252, 54
	v_readlane_b32 s44, v252, 55
	v_readlane_b32 s45, v252, 56
	v_readlane_b32 s46, v252, 57
	v_readlane_b32 s47, v252, 58
	v_readlane_b32 s48, v252, 59
	v_readlane_b32 s49, v252, 60
	v_readlane_b32 s50, v252, 61
	v_readlane_b32 s51, v252, 62
	s_and_saveexec_b64 s[76:77], s[2:3]
	s_cbranch_execz .LBB0_814
	s_waitcnt vmcnt(9)
	v_pk_add_f32 v[184:185], v[2:3], v[4:5]
	v_pk_add_f32 v[186:187], v[6:7], v[8:9]
	v_pk_add_f32 v[184:185], v[184:185], 0 op_sel_hi:[1,0]
	s_mov_b32 s92, 0x3a800000
	v_pk_add_f32 v[184:185], v[184:185], v[186:187]
	v_pk_add_f32 v[186:187], v[10:11], v[12:13]
	s_nop 0
	v_pk_add_f32 v[184:185], v[184:185], v[186:187]
	v_pk_add_f32 v[186:187], v[14:15], v[16:17]
	s_nop 0
	v_pk_add_f32 v[184:185], v[184:185], v[186:187]
	s_waitcnt vmcnt(5)
	v_pk_add_f32 v[186:187], v[18:19], v[20:21]
	s_nop 0
	v_pk_add_f32 v[184:185], v[184:185], v[186:187]
	v_pk_add_f32 v[186:187], v[22:23], v[24:25]
	s_nop 0
	v_pk_add_f32 v[184:185], v[184:185], v[186:187]
	v_pk_add_f32 v[186:187], v[26:27], v[28:29]
	s_nop 0
	v_pk_add_f32 v[184:185], v[184:185], v[186:187]
	v_pk_add_f32 v[186:187], v[30:31], v[32:33]
	s_nop 0
	v_pk_add_f32 v[184:185], v[184:185], v[186:187]
	s_nop 0
	v_pk_mul_f32 v[184:185], v[184:185], s[92:93] op_sel_hi:[1,0]
	s_mov_b32 s92, 0x800000
	v_fma_f32 v155, -v184, v184, v185
	v_max_f32_e32 v155, 0, v155
	v_add_f32_e32 v155, 0x3727c5ac, v155
	v_mul_f32_e32 v157, 0x4b800000, v155
	v_cmp_gt_f32_e32 vcc, s92, v155
	s_nop 1
	v_cndmask_b32_e32 v155, v155, v157, vcc
	v_rsq_f32_e32 v155, v155
	s_nop 0
	v_mul_f32_e32 v157, 0x45800000, v155
	v_cndmask_b32_e32 v185, v155, v157, vcc
	ds_write_b64 v178, v[184:185]
.LBB0_814:
	s_or_b64 exec, exec, s[76:77]
	s_waitcnt vmcnt(3)
	ds_write_b64 v241, v[244:245]
	ds_write_b64 v241, v[246:247] offset:1024
	s_waitcnt lgkmcnt(0)
	s_barrier
	s_add_i32 s98, s90, 16
	s_and_b32 s98, s98, 0xffffff80
	s_add_i32 s99, s33, 0x80
	s_and_b32 s99, s99, 0x380
	s_lshl_b32 s100, s99, 1
	s_mov_b32 s101, 0
	v_add_u32_e32 v200, s98, v177
	v_ashrrev_i32_e32 v201, 31, v200
	v_lshlrev_b64 v[200:201], 11, v[200:201]
	v_lshl_add_u64 v[200:201], s[80:81], 0, v[200:201]
	v_lshl_add_u64 v[200:201], v[200:201], 0, s[100:101]
	v_mov_b32_e32 v202, v154
	v_mov_b32_e32 v203, 0
	v_lshl_add_u64 v[200:201], v[200:201], 0, v[202:203]
	v_add_u32_e32 v204, s98, v176
	v_ashrrev_i32_e32 v205, 31, v204
	v_lshlrev_b64 v[204:205], 11, v[204:205]
	v_lshl_add_u64 v[204:205], s[0:1], 0, v[204:205]
	v_lshl_add_u64 v[204:205], v[204:205], 0, s[100:101]
	v_mov_b32_e32 v202, v156
	v_lshl_add_u64 v[204:205], v[204:205], 0, v[202:203]
	v_lshl_add_u64 v[204:205], v[204:205], 0, v[202:203]
	v_readfirstlane_b32 s98, v0
	s_nop 3
	s_lshr_b32 s98, s98, 6
	s_lshl_b32 s98, s98, 13
	s_add_i32 s98, s98, 0xa800
	v_mov_b32_e32 v206, 16
	v_mov_b32_e32 v207, 0
	v_mov_b32_e32 v208, 64
	v_mov_b32_e32 v209, 0
	s_add_i32 m0, s98, 0xc00
	s_nop 0
	global_load_lds_dwordx4 v[200:201], off
	v_lshl_add_u64 v[200:201], v[200:201], 0, v[206:207]
	s_add_i32 m0, s98, 0x800
	s_nop 0
	global_load_lds_dwordx4 v[200:201], off
	v_lshl_add_u64 v[200:201], v[200:201], 0, v[206:207]
	s_add_i32 m0, s98, 0x400
	s_nop 0
	global_load_lds_dwordx4 v[200:201], off
	v_lshl_add_u64 v[200:201], v[200:201], 0, v[206:207]
	s_add_i32 m0, s98, 0x0
	s_nop 0
	global_load_lds_dwordx4 v[200:201], off
	s_add_i32 m0, s98, 0x1000
	s_nop 0
	global_load_lds_dwordx4 v[204:205], off
	v_lshl_add_u64 v[204:205], v[204:205], 0, v[208:209]
	s_add_i32 m0, s98, 0x1400
	s_nop 0
	global_load_lds_dwordx4 v[204:205], off
	v_lshl_add_u64 v[204:205], v[204:205], 0, v[208:209]
	s_add_i32 m0, s98, 0x1800
	s_nop 0
	global_load_lds_dwordx4 v[204:205], off
	v_lshl_add_u64 v[204:205], v[204:205], 0, v[208:209]
	s_add_i32 m0, s98, 0x1c00
	s_nop 0
	global_load_lds_dwordx4 v[204:205], off
	ds_read_b128 v[138:141], v240
	ds_read_b128 v[126:129], v240 offset:16
	ds_read_b128 v[118:121], v240 offset:32
	ds_read_b128 v[106:109], v240 offset:48
	ds_read_b128 v[98:101], v240 offset:64
	ds_read_b128 v[90:93], v240 offset:80
	ds_read_b128 v[78:81], v240 offset:96
	ds_read_b128 v[66:69], v240 offset:112
	ds_read_b128 v[142:145], v240 offset:1024
	ds_read_b128 v[134:137], v240 offset:1040
	ds_read_b128 v[122:125], v240 offset:1056
	ds_read_b128 v[114:117], v240 offset:1072
	ds_read_b128 v[102:105], v240 offset:1088
	ds_read_b128 v[94:97], v240 offset:1104
	ds_read_b128 v[82:85], v240 offset:1120
	ds_read_b128 v[70:73], v240 offset:1136
	ds_read_b64 v[184:185], v179
	v_lshlrev_b32_e32 v155, 16, v130
	v_and_b32_e32 v130, 0xffff0000, v130
	s_waitcnt vmcnt(10)
	v_cndmask_b32_e64 v62, v62, 0, s[12:13]
	v_cndmask_b32_e64 v63, v63, 0, s[14:15]
	s_waitcnt lgkmcnt(0)
; __device__ __forceinline__ unsigned f2bf(float f) { unsigned u = __builtin_bit_cast(unsigned, f); return (u + 0x7fffu + ((u >> 16) & 1u)) >> 16; }
; __device__ __forceinline__ void sg_phase(const Frame& F, const KArgs& a, const int u_first, const int u_count) {
;     ...
;         { const int s = s_; const f32x2 ms = st[s];
; #pragma unroll
;             for (int q = 0; q < 4; ++q) { const u32x4 raw = zraw[q]; const unsigned rw[4] = {raw.x, raw.y, raw.z, raw.w};
;                 const f32x4 g0 = lg[q][0], g1 = lg[q][1], b0 = lb[q][0], b1 = lb[q][1];
; #pragma unroll
;                 for (int i = 0; i < 8; ++i) { const unsigned wd = rw[i >> 1]; const float v = __builtin_bit_cast(float, (i & 1) ? (wd & 0xffff0000u) : (wd << 16));
;                     const float gg = (i < 4) ? g0[i & 3] : g1[i & 3], bb = (i < 4) ? b0[i & 3] : b1[i & 3];
;                     vt[(c0 + 8 * q + i) * 136 + (s ^ ((tid & 3) * 16))] = (unsigned short)f2bf((v - ms[0]) * ms[1] * gg + bb); } } }
	v_sub_f32_e32 v155, v155, v184
	v_mul_f32_e32 v155, v185, v155
	v_fma_f32 v138, v138, v155, v142
	v_sub_f32_e32 v130, v130, v184
	v_bfe_u32 v142, v138, 16, 1
	v_mul_f32_e32 v130, v185, v130
	v_add3_u32 v138, v138, v142, s91
	v_fma_f32 v130, v139, v130, v143
	ds_write_b16_d16_hi v183, v138 offset:5376
	v_bfe_u32 v138, v130, 16, 1
	v_add3_u32 v130, v130, v138, s91
	ds_write_b16_d16_hi v183, v130 offset:5648
	v_lshlrev_b32_e32 v130, 16, v131
	v_sub_f32_e32 v130, v130, v184
	v_mul_f32_e32 v130, v185, v130
	v_fma_f32 v130, v140, v130, v144
	v_bfe_u32 v138, v130, 16, 1
	v_add3_u32 v130, v130, v138, s91
	ds_write_b16_d16_hi v183, v130 offset:5920
	v_and_b32_e32 v130, 0xffff0000, v131
	v_sub_f32_e32 v130, v130, v184
	v_mul_f32_e32 v130, v185, v130
	v_fmac_f32_e32 v145, v141, v130
	v_bfe_u32 v130, v145, 16, 1
	v_add3_u32 v130, v145, v130, s91
	ds_write_b16_d16_hi v183, v130 offset:6192
	v_lshlrev_b32_e32 v130, 16, v132
	v_sub_f32_e32 v130, v130, v184
	v_mul_f32_e32 v130, v185, v130
	v_fma_f32 v126, v126, v130, v134
	v_bfe_u32 v130, v126, 16, 1
	v_add3_u32 v126, v126, v130, s91
	ds_write_b16_d16_hi v183, v126 offset:1024
	v_and_b32_e32 v126, 0xffff0000, v132
	v_sub_f32_e32 v126, v126, v184
	v_mul_f32_e32 v126, v185, v126
	v_fma_f32 v126, v127, v126, v135
	v_bfe_u32 v127, v126, 16, 1
	v_add3_u32 v126, v126, v127, s91
	ds_write_b16_d16_hi v183, v126 offset:1296
	v_lshlrev_b32_e32 v126, 16, v133
	v_sub_f32_e32 v126, v126, v184
	v_mul_f32_e32 v126, v185, v126
	v_fma_f32 v126, v128, v126, v136
	v_bfe_u32 v127, v126, 16, 1
	v_add3_u32 v126, v126, v127, s91
	ds_write_b16_d16_hi v183, v126 offset:1568
	v_and_b32_e32 v126, 0xffff0000, v133
	v_sub_f32_e32 v126, v126, v184
	v_mul_f32_e32 v126, v185, v126
	v_fmac_f32_e32 v137, v129, v126
	v_bfe_u32 v126, v137, 16, 1
	v_add3_u32 v126, v137, v126, s91
	ds_write_b16_d16_hi v183, v126 offset:1840
	v_lshlrev_b32_e32 v126, 16, v110
	v_sub_f32_e32 v126, v126, v184
	v_mul_f32_e32 v126, v185, v126
	v_and_b32_e32 v110, 0xffff0000, v110
	v_fma_f32 v118, v118, v126, v122
	v_sub_f32_e32 v110, v110, v184
	v_bfe_u32 v122, v118, 16, 1
	v_mul_f32_e32 v110, v185, v110
	v_add3_u32 v118, v118, v122, s91
	v_fma_f32 v110, v119, v110, v123
	ds_write_b16_d16_hi v183, v118 offset:6464
	v_bfe_u32 v118, v110, 16, 1
	v_add3_u32 v110, v110, v118, s91
	ds_write_b16_d16_hi v183, v110 offset:6736
	v_lshlrev_b32_e32 v110, 16, v111
	v_sub_f32_e32 v110, v110, v184
	v_mul_f32_e32 v110, v185, v110
	v_fma_f32 v110, v120, v110, v124
	v_bfe_u32 v118, v110, 16, 1
	v_add3_u32 v110, v110, v118, s91
	ds_write_b16_d16_hi v183, v110 offset:7008
	v_and_b32_e32 v110, 0xffff0000, v111
	v_sub_f32_e32 v110, v110, v184
	v_mul_f32_e32 v110, v185, v110
	v_fmac_f32_e32 v125, v121, v110
	v_bfe_u32 v110, v125, 16, 1
	v_add3_u32 v110, v125, v110, s91
	ds_write_b16_d16_hi v183, v110 offset:7280
	v_lshlrev_b32_e32 v110, 16, v112
	v_sub_f32_e32 v110, v110, v184
	v_mul_f32_e32 v110, v185, v110
	v_fma_f32 v106, v106, v110, v114
	v_bfe_u32 v110, v106, 16, 1
	v_add3_u32 v106, v106, v110, s91
	ds_write_b16_d16_hi v183, v106 offset:2112
	v_and_b32_e32 v106, 0xffff0000, v112
	v_sub_f32_e32 v106, v106, v184
	v_mul_f32_e32 v106, v185, v106
	v_fma_f32 v106, v107, v106, v115
	v_bfe_u32 v107, v106, 16, 1
	v_add3_u32 v106, v106, v107, s91
	ds_write_b16_d16_hi v183, v106 offset:2384
	v_lshlrev_b32_e32 v106, 16, v113
	v_sub_f32_e32 v106, v106, v184
	v_mul_f32_e32 v106, v185, v106
	v_fma_f32 v106, v108, v106, v116
	v_bfe_u32 v107, v106, 16, 1
	v_add3_u32 v106, v106, v107, s91
	ds_write_b16_d16_hi v183, v106 offset:2656
	v_and_b32_e32 v106, 0xffff0000, v113
	v_sub_f32_e32 v106, v106, v184
	v_mul_f32_e32 v106, v185, v106
	v_fmac_f32_e32 v117, v109, v106
	v_bfe_u32 v106, v117, 16, 1
	v_add3_u32 v106, v117, v106, s91
	ds_write_b16_d16_hi v183, v106 offset:2928
	v_lshlrev_b32_e32 v106, 16, v86
	v_sub_f32_e32 v106, v106, v184
	v_mul_f32_e32 v106, v185, v106
	v_and_b32_e32 v86, 0xffff0000, v86
	v_fma_f32 v98, v98, v106, v102
	v_sub_f32_e32 v86, v86, v184
	v_bfe_u32 v102, v98, 16, 1
	v_mul_f32_e32 v86, v185, v86
	v_add3_u32 v98, v98, v102, s91
	v_fma_f32 v86, v99, v86, v103
	ds_write_b16_d16_hi v183, v98 offset:7552
	v_bfe_u32 v98, v86, 16, 1
	v_add3_u32 v86, v86, v98, s91
	ds_write_b16_d16_hi v183, v86 offset:7824
	v_lshlrev_b32_e32 v86, 16, v87
	v_sub_f32_e32 v86, v86, v184
	v_mul_f32_e32 v86, v185, v86
	v_fma_f32 v86, v100, v86, v104
	v_bfe_u32 v98, v86, 16, 1
	v_add3_u32 v86, v86, v98, s91
	ds_write_b16_d16_hi v183, v86 offset:8096
	v_and_b32_e32 v86, 0xffff0000, v87
	v_sub_f32_e32 v86, v86, v184
	v_mul_f32_e32 v86, v185, v86
	v_fmac_f32_e32 v105, v101, v86
	v_bfe_u32 v86, v105, 16, 1
	v_add3_u32 v86, v105, v86, s91
	ds_write_b16_d16_hi v183, v86 offset:8368
	v_lshlrev_b32_e32 v86, 16, v88
	v_sub_f32_e32 v86, v86, v184
	v_mul_f32_e32 v86, v185, v86
	v_fma_f32 v86, v90, v86, v94
	v_bfe_u32 v87, v86, 16, 1
	v_add3_u32 v86, v86, v87, s91
	ds_write_b16_d16_hi v183, v86 offset:3200
	v_and_b32_e32 v86, 0xffff0000, v88
	v_sub_f32_e32 v86, v86, v184
	v_mul_f32_e32 v86, v185, v86
	v_fma_f32 v86, v91, v86, v95
	v_bfe_u32 v87, v86, 16, 1
	v_add3_u32 v86, v86, v87, s91
	ds_write_b16_d16_hi v183, v86 offset:3472
	v_lshlrev_b32_e32 v86, 16, v89
	v_sub_f32_e32 v86, v86, v184
	v_mul_f32_e32 v86, v185, v86
	v_fma_f32 v86, v92, v86, v96
	v_bfe_u32 v87, v86, 16, 1
	v_add3_u32 v86, v86, v87, s91
	ds_write_b16_d16_hi v183, v86 offset:3744
; __device__ __forceinline__ unsigned f2bf(float f) { unsigned u = __builtin_bit_cast(unsigned, f); return (u + 0x7fffu + ((u >> 16) & 1u)) >> 16; }
; #define LAS __attribute__((address_space(3)))
; __device__ __forceinline__ unsigned cvt_pk_bf16(float lo, float hi) { unsigned r; asm volatile("v_cvt_pk_bf16_f32 %0, %1, %2" : "=v"(r) : "v"(lo), "v"(hi)); return r; }
; __device__ __forceinline__ void sg_phase(const Frame& F, const KArgs& a, const int u_first, const int u_count) {
;     ...
;                     vt[(c0 + 8 * q + i) * 136 + (s ^ ((tid & 3) * 16))] = (unsigned short)f2bf((v - ms[0]) * ms[1] * gg + bb); } } }
;         __syncthreads();
;         f32x4 acc[8];
; #pragma unroll
;         for (int j = 0; j < 8; ++j) acc[j] = (f32x4){0.f, 0.f, 0.f, 0.f};
; #pragma unroll
;         for (int ks = 0; ks < 4; ++ks) { if (ks > (w >> 1)) continue;
;             const f32x4 w0 = wraw[ks][0], w1 = wraw[ks][1];
;             float wv[8] = {w0[0], w0[1], w0[2], w0[3], w1[0], w1[1], w1[2], w1[3]};
; #pragma unroll
;             for (int i = 0; i < 8; ++i) if (32 * ks + 8 * kq + i > t) wv[i] = 0.f;
;             u32x4 pk; pk.x = cvt_pk_bf16(wv[0], wv[1]); pk.y = cvt_pk_bf16(wv[2], wv[3]); pk.z = cvt_pk_bf16(wv[4], wv[5]); pk.w = cvt_pk_bf16(wv[6], wv[7]);
;             const bf16x8 wf = __builtin_bit_cast(bf16x8, pk);
; #pragma unroll
;             for (int j = 0; j < 8; ++j) { const bf16x8 vf = *(const LAS bf16x8*)(vt + (16 * j + tl) * 136 + ((32 * ks + 8 * kq) ^ ((j >> 1) * 16)));
;                 acc[j] = __builtin_amdgcn_mfma_f32_16x16x32_bf16(vf, wf, acc[j], 0, 0, 0); }
;         }
	v_and_b32_e32 v86, 0xffff0000, v89
	v_sub_f32_e32 v86, v86, v184
	v_mul_f32_e32 v86, v185, v86
	v_fmac_f32_e32 v97, v93, v86
	v_bfe_u32 v86, v97, 16, 1
	v_add3_u32 v86, v97, v86, s91
	ds_write_b16_d16_hi v183, v86 offset:4016
	v_lshlrev_b32_e32 v86, 16, v58
	v_sub_f32_e32 v86, v86, v184
	v_mul_f32_e32 v86, v185, v86
	v_and_b32_e32 v58, 0xffff0000, v58
	v_fma_f32 v78, v78, v86, v82
	v_sub_f32_e32 v58, v58, v184
	v_bfe_u32 v82, v78, 16, 1
	v_mul_f32_e32 v58, v185, v58
	v_add3_u32 v78, v78, v82, s91
	v_fma_f32 v58, v79, v58, v83
	ds_write_b16_d16_hi v183, v78 offset:8640
	v_bfe_u32 v78, v58, 16, 1
	v_add3_u32 v58, v58, v78, s91
	ds_write_b16_d16_hi v183, v58 offset:8912
	v_lshlrev_b32_e32 v58, 16, v59
	v_sub_f32_e32 v58, v58, v184
	v_mul_f32_e32 v58, v185, v58
	v_fma_f32 v58, v80, v58, v84
	v_bfe_u32 v78, v58, 16, 1
	v_add3_u32 v58, v58, v78, s91
	ds_write_b16_d16_hi v183, v58 offset:9184
	v_and_b32_e32 v58, 0xffff0000, v59
	v_sub_f32_e32 v58, v58, v184
	v_mul_f32_e32 v58, v185, v58
	v_fmac_f32_e32 v85, v81, v58
	v_bfe_u32 v58, v85, 16, 1
	v_add3_u32 v58, v85, v58, s91
	ds_write_b16_d16_hi v183, v58 offset:9456
	v_lshlrev_b32_e32 v58, 16, v60
	v_sub_f32_e32 v58, v58, v184
	v_mul_f32_e32 v58, v185, v58
	v_fma_f32 v58, v66, v58, v70
	v_bfe_u32 v59, v58, 16, 1
	v_add3_u32 v58, v58, v59, s91
	ds_write_b16_d16_hi v183, v58 offset:4288
	v_and_b32_e32 v58, 0xffff0000, v60
	v_sub_f32_e32 v58, v58, v184
	v_mul_f32_e32 v58, v185, v58
	v_fma_f32 v58, v67, v58, v71
	v_bfe_u32 v59, v58, 16, 1
	v_add3_u32 v58, v58, v59, s91
	ds_write_b16_d16_hi v183, v58 offset:4560
	v_lshlrev_b32_e32 v58, 16, v61
	v_sub_f32_e32 v58, v58, v184
	v_mul_f32_e32 v58, v185, v58
	v_fma_f32 v58, v68, v58, v72
	v_bfe_u32 v59, v58, 16, 1
	v_add3_u32 v58, v58, v59, s91
	ds_write_b16_d16_hi v183, v58 offset:4832
	v_and_b32_e32 v58, 0xffff0000, v61
	v_sub_f32_e32 v58, v58, v184
	v_mul_f32_e32 v58, v185, v58
	v_fmac_f32_e32 v73, v69, v58
	v_bfe_u32 v58, v73, 16, 1
	v_add3_u32 v58, v73, v58, s91
	ds_write_b16_d16_hi v183, v58 offset:5104
	s_waitcnt vmcnt(9)
	v_cndmask_b32_e64 v58, v74, 0, s[4:5]
	v_cndmask_b32_e64 v59, 0, v75, s[6:7]
	v_cndmask_b32_e64 v58, v58, v74, s[6:7]
	v_cndmask_b32_e64 v60, v76, 0, s[8:9]
	v_cndmask_b32_e64 v61, v77, 0, s[10:11]
	v_cndmask_b32_e64 v64, v64, 0, s[16:17]
	v_cndmask_b32_e64 v65, v65, 0, s[18:19]
	s_waitcnt lgkmcnt(0)
	s_barrier
	v_cvt_pk_bf16_f32 v58, v58, v59
	v_cvt_pk_bf16_f32 v59, v60, v61
	v_cvt_pk_bf16_f32 v60, v62, v63
	v_cvt_pk_bf16_f32 v61, v64, v65
	ds_read_b128 v[62:65], v180 offset:1024
	ds_read_b128 v[66:69], v180 offset:5376
	s_waitcnt lgkmcnt(1)
	v_mfma_f32_16x16x32_bf16 v[86:89], v[62:65], v[58:61], 0
	ds_read_b128 v[62:65], v181 offset:9728
	ds_read_b128 v[90:93], v181 offset:31552
	s_and_b64 vcc, exec, s[74:75]
	s_waitcnt lgkmcnt(2)
	v_mfma_f32_16x16x32_bf16 v[82:85], v[66:69], v[58:61], 0
	ds_read_b128 v[66:69], v181 offset:14080
	s_waitcnt lgkmcnt(2)
	v_mfma_f32_16x16x32_bf16 v[78:81], v[62:65], v[58:61], 0
	ds_read_b128 v[62:65], v180 offset:18496
	s_waitcnt lgkmcnt(1)
	v_mfma_f32_16x16x32_bf16 v[74:77], v[66:69], v[58:61], 0
	ds_read_b128 v[66:69], v180 offset:22848
	s_waitcnt lgkmcnt(1)
	v_mfma_f32_16x16x32_bf16 v[70:73], v[62:65], v[58:61], 0
	ds_read_b128 v[62:65], v181 offset:27200
	s_waitcnt lgkmcnt(1)
	v_mfma_f32_16x16x32_bf16 v[66:69], v[66:69], v[58:61], 0
	s_waitcnt lgkmcnt(0)
	v_mfma_f32_16x16x32_bf16 v[62:65], v[62:65], v[58:61], 0
	v_mfma_f32_16x16x32_bf16 v[58:61], v[90:93], v[58:61], 0
	s_cbranch_vccnz .LBB0_816
	v_readlane_b32 s36, v251, 7
	v_readlane_b32 s37, v251, 8
	v_cndmask_b32_e64 v53, v53, 0, s[94:95]
	v_cndmask_b32_e64 v92, v52, 0, s[34:35]
	v_cndmask_b32_e64 v54, v54, 0, s[36:37]
	v_readlane_b32 s36, v251, 16
	v_readlane_b32 s37, v251, 17
	s_nop 1
	v_cndmask_b32_e64 v55, v55, 0, s[36:37]
	v_readlane_b32 s36, v251, 22
	v_readlane_b32 s37, v251, 23
	s_nop 1
	v_cndmask_b32_e64 v56, v56, 0, s[36:37]
	v_readlane_b32 s36, v251, 24
	v_readlane_b32 s37, v251, 25
	s_nop 1
	v_cndmask_b32_e64 v57, v57, 0, s[36:37]
	v_readlane_b32 s36, v251, 26
	v_readlane_b32 s37, v251, 27
	s_nop 1
	v_cndmask_b32_e64 v90, v50, 0, s[36:37]
	v_readlane_b32 s36, v251, 28
	v_readlane_b32 s37, v251, 29
	v_cvt_pk_bf16_f32 v50, v54, v55
	s_nop 1
	v_cndmask_b32_e64 v91, v51, 0, s[36:37]
	v_cvt_pk_bf16_f32 v51, v56, v57
	v_cvt_pk_bf16_f32 v52, v90, v91
	v_cvt_pk_bf16_f32 v53, v92, v53
	ds_read_b128 v[2:5], v180 offset:1088
	ds_read_b128 v[6:9], v180 offset:5440
	ds_read_b128 v[10:13], v181 offset:9792
	ds_read_b128 v[14:17], v181 offset:14144
	ds_read_b128 v[18:21], v180 offset:18432
	ds_read_b128 v[22:25], v180 offset:22784
	ds_read_b128 v[26:29], v181 offset:27136
	ds_read_b128 v[30:33], v181 offset:31488
	s_waitcnt lgkmcnt(7)
	v_mfma_f32_16x16x32_bf16 v[86:89], v[2:5], v[50:53], v[86:89]
	s_waitcnt lgkmcnt(6)
	v_mfma_f32_16x16x32_bf16 v[82:85], v[6:9], v[50:53], v[82:85]
	s_waitcnt lgkmcnt(5)
	v_mfma_f32_16x16x32_bf16 v[78:81], v[10:13], v[50:53], v[78:81]
	s_waitcnt lgkmcnt(4)
	v_mfma_f32_16x16x32_bf16 v[74:77], v[14:17], v[50:53], v[74:77]
	s_waitcnt lgkmcnt(3)
	v_mfma_f32_16x16x32_bf16 v[70:73], v[18:21], v[50:53], v[70:73]
	s_waitcnt lgkmcnt(2)
	v_mfma_f32_16x16x32_bf16 v[66:69], v[22:25], v[50:53], v[66:69]
	s_waitcnt lgkmcnt(1)
	v_mfma_f32_16x16x32_bf16 v[62:65], v[26:29], v[50:53], v[62:65]
	s_waitcnt lgkmcnt(0)
	v_mfma_f32_16x16x32_bf16 v[58:61], v[30:33], v[50:53], v[58:61]
